# combine phase split-K remainder rows: slab partial sums with all S load pairs in flight (guarded unroll) instead of one pair per round trip
# baseline (speedup 1.0000x reference)
.LBB0_4025:
	global_load_dwordx4 v[64:67], v[6:7], off
	global_load_dwordx4 v[68:71], v[6:7], off offset:16
	s_cmp_lt_u32 s2, 2
	s_cbranch_scc1 .Lslab0_w
	v_lshl_add_u64 v[6:7], v[6:7], 0, s[10:11]
	global_load_dwordx4 v[72:75], v[6:7], off
	global_load_dwordx4 v[76:79], v[6:7], off offset:16
	s_cmp_lt_u32 s2, 3
	s_cbranch_scc1 .Lslab0_w
	v_lshl_add_u64 v[6:7], v[6:7], 0, s[10:11]
	global_load_dwordx4 v[80:83], v[6:7], off
	global_load_dwordx4 v[84:87], v[6:7], off offset:16
	s_cmp_lt_u32 s2, 4
	s_cbranch_scc1 .Lslab0_w
	v_lshl_add_u64 v[6:7], v[6:7], 0, s[10:11]
	global_load_dwordx4 v[88:91], v[6:7], off
	global_load_dwordx4 v[92:95], v[6:7], off offset:16
	s_cmp_lt_u32 s2, 5
	s_cbranch_scc1 .Lslab0_w
	v_lshl_add_u64 v[6:7], v[6:7], 0, s[10:11]
	global_load_dwordx4 v[96:99], v[6:7], off
	global_load_dwordx4 v[100:103], v[6:7], off offset:16
	s_cmp_lt_u32 s2, 6
	s_cbranch_scc1 .Lslab0_w
	v_lshl_add_u64 v[6:7], v[6:7], 0, s[10:11]
	global_load_dwordx4 v[104:107], v[6:7], off
	global_load_dwordx4 v[108:111], v[6:7], off offset:16
	s_cmp_lt_u32 s2, 7
	s_cbranch_scc1 .Lslab0_w
	v_lshl_add_u64 v[6:7], v[6:7], 0, s[10:11]
	global_load_dwordx4 v[112:115], v[6:7], off
	global_load_dwordx4 v[116:119], v[6:7], off offset:16
	s_cmp_lt_u32 s2, 8
	s_cbranch_scc1 .Lslab0_w
	v_lshl_add_u64 v[6:7], v[6:7], 0, s[10:11]
	global_load_dwordx4 v[120:123], v[6:7], off
	global_load_dwordx4 v[124:127], v[6:7], off offset:16
	s_cmp_lt_u32 s2, 9
	s_cbranch_scc1 .Lslab0_w
	v_lshl_add_u64 v[6:7], v[6:7], 0, s[10:11]
	global_load_dwordx4 v[128:131], v[6:7], off
	global_load_dwordx4 v[132:135], v[6:7], off offset:16
	s_cmp_lt_u32 s2, 10
	s_cbranch_scc1 .Lslab0_w
	v_lshl_add_u64 v[6:7], v[6:7], 0, s[10:11]
	global_load_dwordx4 v[136:139], v[6:7], off
	global_load_dwordx4 v[140:143], v[6:7], off offset:16
	s_cmp_lt_u32 s2, 11
	s_cbranch_scc1 .Lslab0_w
	v_lshl_add_u64 v[6:7], v[6:7], 0, s[10:11]
	global_load_dwordx4 v[144:147], v[6:7], off
	global_load_dwordx4 v[148:151], v[6:7], off offset:16
	s_cmp_lt_u32 s2, 12
	s_cbranch_scc1 .Lslab0_w
	v_lshl_add_u64 v[6:7], v[6:7], 0, s[10:11]
	global_load_dwordx4 v[152:155], v[6:7], off
	global_load_dwordx4 v[156:159], v[6:7], off offset:16
	s_cmp_lt_u32 s2, 13
	s_cbranch_scc1 .Lslab0_w
	v_lshl_add_u64 v[6:7], v[6:7], 0, s[10:11]
	global_load_dwordx4 v[160:163], v[6:7], off
	global_load_dwordx4 v[164:167], v[6:7], off offset:16
	s_cmp_lt_u32 s2, 14
	s_cbranch_scc1 .Lslab0_w
	v_lshl_add_u64 v[6:7], v[6:7], 0, s[10:11]
	global_load_dwordx4 v[168:171], v[6:7], off
	global_load_dwordx4 v[172:175], v[6:7], off offset:16
.Lslab0_w:
	s_waitcnt vmcnt(0)
	v_pk_add_f32 v[4:5], v[4:5], v[66:67]
	v_pk_add_f32 v[8:9], v[8:9], v[64:65]
	v_pk_add_f32 v[2:3], v[2:3], v[70:71]
	v_pk_add_f32 v[0:1], v[0:1], v[68:69]
	s_cmp_lt_u32 s2, 2
	s_cbranch_scc1 .Lslab0_d
	v_pk_add_f32 v[4:5], v[4:5], v[74:75]
	v_pk_add_f32 v[8:9], v[8:9], v[72:73]
	v_pk_add_f32 v[2:3], v[2:3], v[78:79]
	v_pk_add_f32 v[0:1], v[0:1], v[76:77]
	s_cmp_lt_u32 s2, 3
	s_cbranch_scc1 .Lslab0_d
	v_pk_add_f32 v[4:5], v[4:5], v[82:83]
	v_pk_add_f32 v[8:9], v[8:9], v[80:81]
	v_pk_add_f32 v[2:3], v[2:3], v[86:87]
	v_pk_add_f32 v[0:1], v[0:1], v[84:85]
	s_cmp_lt_u32 s2, 4
	s_cbranch_scc1 .Lslab0_d
	v_pk_add_f32 v[4:5], v[4:5], v[90:91]
	v_pk_add_f32 v[8:9], v[8:9], v[88:89]
	v_pk_add_f32 v[2:3], v[2:3], v[94:95]
	v_pk_add_f32 v[0:1], v[0:1], v[92:93]
	s_cmp_lt_u32 s2, 5
	s_cbranch_scc1 .Lslab0_d
	v_pk_add_f32 v[4:5], v[4:5], v[98:99]
	v_pk_add_f32 v[8:9], v[8:9], v[96:97]
	v_pk_add_f32 v[2:3], v[2:3], v[102:103]
	v_pk_add_f32 v[0:1], v[0:1], v[100:101]
	s_cmp_lt_u32 s2, 6
	s_cbranch_scc1 .Lslab0_d
	v_pk_add_f32 v[4:5], v[4:5], v[106:107]
	v_pk_add_f32 v[8:9], v[8:9], v[104:105]
	v_pk_add_f32 v[2:3], v[2:3], v[110:111]
	v_pk_add_f32 v[0:1], v[0:1], v[108:109]
	s_cmp_lt_u32 s2, 7
	s_cbranch_scc1 .Lslab0_d
	v_pk_add_f32 v[4:5], v[4:5], v[114:115]
	v_pk_add_f32 v[8:9], v[8:9], v[112:113]
	v_pk_add_f32 v[2:3], v[2:3], v[118:119]
	v_pk_add_f32 v[0:1], v[0:1], v[116:117]
	s_cmp_lt_u32 s2, 8
	s_cbranch_scc1 .Lslab0_d
	v_pk_add_f32 v[4:5], v[4:5], v[122:123]
	v_pk_add_f32 v[8:9], v[8:9], v[120:121]
	v_pk_add_f32 v[2:3], v[2:3], v[126:127]
	v_pk_add_f32 v[0:1], v[0:1], v[124:125]
	s_cmp_lt_u32 s2, 9
	s_cbranch_scc1 .Lslab0_d
	v_pk_add_f32 v[4:5], v[4:5], v[130:131]
	v_pk_add_f32 v[8:9], v[8:9], v[128:129]
	v_pk_add_f32 v[2:3], v[2:3], v[134:135]
	v_pk_add_f32 v[0:1], v[0:1], v[132:133]
	s_cmp_lt_u32 s2, 10
	s_cbranch_scc1 .Lslab0_d
	v_pk_add_f32 v[4:5], v[4:5], v[138:139]
	v_pk_add_f32 v[8:9], v[8:9], v[136:137]
	v_pk_add_f32 v[2:3], v[2:3], v[142:143]
	v_pk_add_f32 v[0:1], v[0:1], v[140:141]
	s_cmp_lt_u32 s2, 11
	s_cbranch_scc1 .Lslab0_d
	v_pk_add_f32 v[4:5], v[4:5], v[146:147]
	v_pk_add_f32 v[8:9], v[8:9], v[144:145]
	v_pk_add_f32 v[2:3], v[2:3], v[150:151]
	v_pk_add_f32 v[0:1], v[0:1], v[148:149]
	s_cmp_lt_u32 s2, 12
	s_cbranch_scc1 .Lslab0_d
	v_pk_add_f32 v[4:5], v[4:5], v[154:155]
	v_pk_add_f32 v[8:9], v[8:9], v[152:153]
	v_pk_add_f32 v[2:3], v[2:3], v[158:159]
	v_pk_add_f32 v[0:1], v[0:1], v[156:157]
	s_cmp_lt_u32 s2, 13
	s_cbranch_scc1 .Lslab0_d
	v_pk_add_f32 v[4:5], v[4:5], v[162:163]
	v_pk_add_f32 v[8:9], v[8:9], v[160:161]
	v_pk_add_f32 v[2:3], v[2:3], v[166:167]
	v_pk_add_f32 v[0:1], v[0:1], v[164:165]
	s_cmp_lt_u32 s2, 14
	s_cbranch_scc1 .Lslab0_d
	v_pk_add_f32 v[4:5], v[4:5], v[170:171]
	v_pk_add_f32 v[8:9], v[8:9], v[168:169]
	v_pk_add_f32 v[2:3], v[2:3], v[174:175]
	v_pk_add_f32 v[0:1], v[0:1], v[172:173]
.Lslab0_d:
	s_mov_b32 s2, 0
	s_cmp_eq_u32 s2, 0
	v_pk_mul_f32 v[6:7], v[2:3], s[12:13] op_sel_hi:[1,0]
	v_pk_mul_f32 v[2:3], v[4:5], s[12:13] op_sel_hi:[1,0]
	v_pk_mul_f32 v[4:5], v[0:1], s[12:13] op_sel_hi:[1,0]
	v_pk_mul_f32 v[0:1], v[8:9], s[12:13] op_sel_hi:[1,0]
	s_mov_b64 s[2:3], 0

.LBB0_4031:
	global_load_dwordx4 v[64:67], v[14:15], off
	global_load_dwordx4 v[68:71], v[14:15], off offset:16
	s_cmp_lt_u32 s2, 2
	s_cbranch_scc1 .Lslab1_w
	v_lshl_add_u64 v[14:15], v[14:15], 0, s[10:11]
	global_load_dwordx4 v[72:75], v[14:15], off
	global_load_dwordx4 v[76:79], v[14:15], off offset:16
	s_cmp_lt_u32 s2, 3
	s_cbranch_scc1 .Lslab1_w
	v_lshl_add_u64 v[14:15], v[14:15], 0, s[10:11]
	global_load_dwordx4 v[80:83], v[14:15], off
	global_load_dwordx4 v[84:87], v[14:15], off offset:16
	s_cmp_lt_u32 s2, 4
	s_cbranch_scc1 .Lslab1_w
	v_lshl_add_u64 v[14:15], v[14:15], 0, s[10:11]
	global_load_dwordx4 v[88:91], v[14:15], off
	global_load_dwordx4 v[92:95], v[14:15], off offset:16
	s_cmp_lt_u32 s2, 5
	s_cbranch_scc1 .Lslab1_w
	v_lshl_add_u64 v[14:15], v[14:15], 0, s[10:11]
	global_load_dwordx4 v[96:99], v[14:15], off
	global_load_dwordx4 v[100:103], v[14:15], off offset:16
	s_cmp_lt_u32 s2, 6
	s_cbranch_scc1 .Lslab1_w
	v_lshl_add_u64 v[14:15], v[14:15], 0, s[10:11]
	global_load_dwordx4 v[104:107], v[14:15], off
	global_load_dwordx4 v[108:111], v[14:15], off offset:16
	s_cmp_lt_u32 s2, 7
	s_cbranch_scc1 .Lslab1_w
	v_lshl_add_u64 v[14:15], v[14:15], 0, s[10:11]
	global_load_dwordx4 v[112:115], v[14:15], off
	global_load_dwordx4 v[116:119], v[14:15], off offset:16
	s_cmp_lt_u32 s2, 8
	s_cbranch_scc1 .Lslab1_w
	v_lshl_add_u64 v[14:15], v[14:15], 0, s[10:11]
	global_load_dwordx4 v[120:123], v[14:15], off
	global_load_dwordx4 v[124:127], v[14:15], off offset:16
	s_cmp_lt_u32 s2, 9
	s_cbranch_scc1 .Lslab1_w
	v_lshl_add_u64 v[14:15], v[14:15], 0, s[10:11]
	global_load_dwordx4 v[128:131], v[14:15], off
	global_load_dwordx4 v[132:135], v[14:15], off offset:16
	s_cmp_lt_u32 s2, 10
	s_cbranch_scc1 .Lslab1_w
	v_lshl_add_u64 v[14:15], v[14:15], 0, s[10:11]
	global_load_dwordx4 v[136:139], v[14:15], off
	global_load_dwordx4 v[140:143], v[14:15], off offset:16
	s_cmp_lt_u32 s2, 11
	s_cbranch_scc1 .Lslab1_w
	v_lshl_add_u64 v[14:15], v[14:15], 0, s[10:11]
	global_load_dwordx4 v[144:147], v[14:15], off
	global_load_dwordx4 v[148:151], v[14:15], off offset:16
	s_cmp_lt_u32 s2, 12
	s_cbranch_scc1 .Lslab1_w
	v_lshl_add_u64 v[14:15], v[14:15], 0, s[10:11]
	global_load_dwordx4 v[152:155], v[14:15], off
	global_load_dwordx4 v[156:159], v[14:15], off offset:16
	s_cmp_lt_u32 s2, 13
	s_cbranch_scc1 .Lslab1_w
	v_lshl_add_u64 v[14:15], v[14:15], 0, s[10:11]
	global_load_dwordx4 v[160:163], v[14:15], off
	global_load_dwordx4 v[164:167], v[14:15], off offset:16
	s_cmp_lt_u32 s2, 14
	s_cbranch_scc1 .Lslab1_w
	v_lshl_add_u64 v[14:15], v[14:15], 0, s[10:11]
	global_load_dwordx4 v[168:171], v[14:15], off
	global_load_dwordx4 v[172:175], v[14:15], off offset:16
.Lslab1_w:
	s_waitcnt vmcnt(0)
	v_pk_add_f32 v[12:13], v[12:13], v[66:67]
	v_pk_add_f32 v[16:17], v[16:17], v[64:65]
	v_pk_add_f32 v[10:11], v[10:11], v[70:71]
	v_pk_add_f32 v[8:9], v[8:9], v[68:69]
	s_cmp_lt_u32 s2, 2
	s_cbranch_scc1 .Lslab1_d
	v_pk_add_f32 v[12:13], v[12:13], v[74:75]
	v_pk_add_f32 v[16:17], v[16:17], v[72:73]
	v_pk_add_f32 v[10:11], v[10:11], v[78:79]
	v_pk_add_f32 v[8:9], v[8:9], v[76:77]
	s_cmp_lt_u32 s2, 3
	s_cbranch_scc1 .Lslab1_d
	v_pk_add_f32 v[12:13], v[12:13], v[82:83]
	v_pk_add_f32 v[16:17], v[16:17], v[80:81]
	v_pk_add_f32 v[10:11], v[10:11], v[86:87]
	v_pk_add_f32 v[8:9], v[8:9], v[84:85]
	s_cmp_lt_u32 s2, 4
	s_cbranch_scc1 .Lslab1_d
	v_pk_add_f32 v[12:13], v[12:13], v[90:91]
	v_pk_add_f32 v[16:17], v[16:17], v[88:89]
	v_pk_add_f32 v[10:11], v[10:11], v[94:95]
	v_pk_add_f32 v[8:9], v[8:9], v[92:93]
	s_cmp_lt_u32 s2, 5
	s_cbranch_scc1 .Lslab1_d
	v_pk_add_f32 v[12:13], v[12:13], v[98:99]
	v_pk_add_f32 v[16:17], v[16:17], v[96:97]
	v_pk_add_f32 v[10:11], v[10:11], v[102:103]
	v_pk_add_f32 v[8:9], v[8:9], v[100:101]
	s_cmp_lt_u32 s2, 6
	s_cbranch_scc1 .Lslab1_d
	v_pk_add_f32 v[12:13], v[12:13], v[106:107]
	v_pk_add_f32 v[16:17], v[16:17], v[104:105]
	v_pk_add_f32 v[10:11], v[10:11], v[110:111]
	v_pk_add_f32 v[8:9], v[8:9], v[108:109]
	s_cmp_lt_u32 s2, 7
	s_cbranch_scc1 .Lslab1_d
	v_pk_add_f32 v[12:13], v[12:13], v[114:115]
	v_pk_add_f32 v[16:17], v[16:17], v[112:113]
	v_pk_add_f32 v[10:11], v[10:11], v[118:119]
	v_pk_add_f32 v[8:9], v[8:9], v[116:117]
	s_cmp_lt_u32 s2, 8
	s_cbranch_scc1 .Lslab1_d
	v_pk_add_f32 v[12:13], v[12:13], v[122:123]
	v_pk_add_f32 v[16:17], v[16:17], v[120:121]
	v_pk_add_f32 v[10:11], v[10:11], v[126:127]
	v_pk_add_f32 v[8:9], v[8:9], v[124:125]
	s_cmp_lt_u32 s2, 9
	s_cbranch_scc1 .Lslab1_d
	v_pk_add_f32 v[12:13], v[12:13], v[130:131]
	v_pk_add_f32 v[16:17], v[16:17], v[128:129]
	v_pk_add_f32 v[10:11], v[10:11], v[134:135]
	v_pk_add_f32 v[8:9], v[8:9], v[132:133]
	s_cmp_lt_u32 s2, 10
	s_cbranch_scc1 .Lslab1_d
	v_pk_add_f32 v[12:13], v[12:13], v[138:139]
	v_pk_add_f32 v[16:17], v[16:17], v[136:137]
	v_pk_add_f32 v[10:11], v[10:11], v[142:143]
	v_pk_add_f32 v[8:9], v[8:9], v[140:141]
	s_cmp_lt_u32 s2, 11
	s_cbranch_scc1 .Lslab1_d
	v_pk_add_f32 v[12:13], v[12:13], v[146:147]
	v_pk_add_f32 v[16:17], v[16:17], v[144:145]
	v_pk_add_f32 v[10:11], v[10:11], v[150:151]
	v_pk_add_f32 v[8:9], v[8:9], v[148:149]
	s_cmp_lt_u32 s2, 12
	s_cbranch_scc1 .Lslab1_d
	v_pk_add_f32 v[12:13], v[12:13], v[154:155]
	v_pk_add_f32 v[16:17], v[16:17], v[152:153]
	v_pk_add_f32 v[10:11], v[10:11], v[158:159]
	v_pk_add_f32 v[8:9], v[8:9], v[156:157]
	s_cmp_lt_u32 s2, 13
	s_cbranch_scc1 .Lslab1_d
	v_pk_add_f32 v[12:13], v[12:13], v[162:163]
	v_pk_add_f32 v[16:17], v[16:17], v[160:161]
	v_pk_add_f32 v[10:11], v[10:11], v[166:167]
	v_pk_add_f32 v[8:9], v[8:9], v[164:165]
	s_cmp_lt_u32 s2, 14
	s_cbranch_scc1 .Lslab1_d
	v_pk_add_f32 v[12:13], v[12:13], v[170:171]
	v_pk_add_f32 v[16:17], v[16:17], v[168:169]
	v_pk_add_f32 v[10:11], v[10:11], v[174:175]
	v_pk_add_f32 v[8:9], v[8:9], v[172:173]
.Lslab1_d:
	s_mov_b32 s2, 0
	s_cmp_eq_u32 s2, 0
	v_pk_mul_f32 v[14:15], v[10:11], s[12:13] op_sel_hi:[1,0]
	v_pk_mul_f32 v[10:11], v[12:13], s[12:13] op_sel_hi:[1,0]
	v_pk_mul_f32 v[12:13], v[8:9], s[12:13] op_sel_hi:[1,0]
	v_pk_mul_f32 v[8:9], v[16:17], s[12:13] op_sel_hi:[1,0]
	s_mov_b64 s[2:3], 0

.LBB0_4037:
	global_load_dwordx4 v[64:67], v[6:7], off
	global_load_dwordx4 v[68:71], v[6:7], off offset:16
	s_cmp_lt_u32 s0, 2
	s_cbranch_scc1 .Lslab2_w
	v_lshl_add_u64 v[6:7], v[6:7], 0, s[10:11]
	global_load_dwordx4 v[72:75], v[6:7], off
	global_load_dwordx4 v[76:79], v[6:7], off offset:16
	s_cmp_lt_u32 s0, 3
	s_cbranch_scc1 .Lslab2_w
	v_lshl_add_u64 v[6:7], v[6:7], 0, s[10:11]
	global_load_dwordx4 v[80:83], v[6:7], off
	global_load_dwordx4 v[84:87], v[6:7], off offset:16
	s_cmp_lt_u32 s0, 4
	s_cbranch_scc1 .Lslab2_w
	v_lshl_add_u64 v[6:7], v[6:7], 0, s[10:11]
	global_load_dwordx4 v[88:91], v[6:7], off
	global_load_dwordx4 v[92:95], v[6:7], off offset:16
	s_cmp_lt_u32 s0, 5
	s_cbranch_scc1 .Lslab2_w
	v_lshl_add_u64 v[6:7], v[6:7], 0, s[10:11]
	global_load_dwordx4 v[96:99], v[6:7], off
	global_load_dwordx4 v[100:103], v[6:7], off offset:16
	s_cmp_lt_u32 s0, 6
	s_cbranch_scc1 .Lslab2_w
	v_lshl_add_u64 v[6:7], v[6:7], 0, s[10:11]
	global_load_dwordx4 v[104:107], v[6:7], off
	global_load_dwordx4 v[108:111], v[6:7], off offset:16
	s_cmp_lt_u32 s0, 7
	s_cbranch_scc1 .Lslab2_w
	v_lshl_add_u64 v[6:7], v[6:7], 0, s[10:11]
	global_load_dwordx4 v[112:115], v[6:7], off
	global_load_dwordx4 v[116:119], v[6:7], off offset:16
	s_cmp_lt_u32 s0, 8
	s_cbranch_scc1 .Lslab2_w
	v_lshl_add_u64 v[6:7], v[6:7], 0, s[10:11]
	global_load_dwordx4 v[120:123], v[6:7], off
	global_load_dwordx4 v[124:127], v[6:7], off offset:16
	s_cmp_lt_u32 s0, 9
	s_cbranch_scc1 .Lslab2_w
	v_lshl_add_u64 v[6:7], v[6:7], 0, s[10:11]
	global_load_dwordx4 v[128:131], v[6:7], off
	global_load_dwordx4 v[132:135], v[6:7], off offset:16
	s_cmp_lt_u32 s0, 10
	s_cbranch_scc1 .Lslab2_w
	v_lshl_add_u64 v[6:7], v[6:7], 0, s[10:11]
	global_load_dwordx4 v[136:139], v[6:7], off
	global_load_dwordx4 v[140:143], v[6:7], off offset:16
	s_cmp_lt_u32 s0, 11
	s_cbranch_scc1 .Lslab2_w
	v_lshl_add_u64 v[6:7], v[6:7], 0, s[10:11]
	global_load_dwordx4 v[144:147], v[6:7], off
	global_load_dwordx4 v[148:151], v[6:7], off offset:16
	s_cmp_lt_u32 s0, 12
	s_cbranch_scc1 .Lslab2_w
	v_lshl_add_u64 v[6:7], v[6:7], 0, s[10:11]
	global_load_dwordx4 v[152:155], v[6:7], off
	global_load_dwordx4 v[156:159], v[6:7], off offset:16
	s_cmp_lt_u32 s0, 13
	s_cbranch_scc1 .Lslab2_w
	v_lshl_add_u64 v[6:7], v[6:7], 0, s[10:11]
	global_load_dwordx4 v[160:163], v[6:7], off
	global_load_dwordx4 v[164:167], v[6:7], off offset:16
	s_cmp_lt_u32 s0, 14
	s_cbranch_scc1 .Lslab2_w
	v_lshl_add_u64 v[6:7], v[6:7], 0, s[10:11]
	global_load_dwordx4 v[168:171], v[6:7], off
	global_load_dwordx4 v[172:175], v[6:7], off offset:16
.Lslab2_w:
	s_waitcnt vmcnt(0)
	v_pk_add_f32 v[4:5], v[4:5], v[66:67]
	v_pk_add_f32 v[8:9], v[8:9], v[64:65]
	v_pk_add_f32 v[2:3], v[2:3], v[70:71]
	v_pk_add_f32 v[0:1], v[0:1], v[68:69]
	s_cmp_lt_u32 s0, 2
	s_cbranch_scc1 .Lslab2_d
	v_pk_add_f32 v[4:5], v[4:5], v[74:75]
	v_pk_add_f32 v[8:9], v[8:9], v[72:73]
	v_pk_add_f32 v[2:3], v[2:3], v[78:79]
	v_pk_add_f32 v[0:1], v[0:1], v[76:77]
	s_cmp_lt_u32 s0, 3
	s_cbranch_scc1 .Lslab2_d
	v_pk_add_f32 v[4:5], v[4:5], v[82:83]
	v_pk_add_f32 v[8:9], v[8:9], v[80:81]
	v_pk_add_f32 v[2:3], v[2:3], v[86:87]
	v_pk_add_f32 v[0:1], v[0:1], v[84:85]
	s_cmp_lt_u32 s0, 4
	s_cbranch_scc1 .Lslab2_d
	v_pk_add_f32 v[4:5], v[4:5], v[90:91]
	v_pk_add_f32 v[8:9], v[8:9], v[88:89]
	v_pk_add_f32 v[2:3], v[2:3], v[94:95]
	v_pk_add_f32 v[0:1], v[0:1], v[92:93]
	s_cmp_lt_u32 s0, 5
	s_cbranch_scc1 .Lslab2_d
	v_pk_add_f32 v[4:5], v[4:5], v[98:99]
	v_pk_add_f32 v[8:9], v[8:9], v[96:97]
	v_pk_add_f32 v[2:3], v[2:3], v[102:103]
	v_pk_add_f32 v[0:1], v[0:1], v[100:101]
	s_cmp_lt_u32 s0, 6
	s_cbranch_scc1 .Lslab2_d
	v_pk_add_f32 v[4:5], v[4:5], v[106:107]
	v_pk_add_f32 v[8:9], v[8:9], v[104:105]
	v_pk_add_f32 v[2:3], v[2:3], v[110:111]
	v_pk_add_f32 v[0:1], v[0:1], v[108:109]
	s_cmp_lt_u32 s0, 7
	s_cbranch_scc1 .Lslab2_d
	v_pk_add_f32 v[4:5], v[4:5], v[114:115]
	v_pk_add_f32 v[8:9], v[8:9], v[112:113]
	v_pk_add_f32 v[2:3], v[2:3], v[118:119]
	v_pk_add_f32 v[0:1], v[0:1], v[116:117]
	s_cmp_lt_u32 s0, 8
	s_cbranch_scc1 .Lslab2_d
	v_pk_add_f32 v[4:5], v[4:5], v[122:123]
	v_pk_add_f32 v[8:9], v[8:9], v[120:121]
	v_pk_add_f32 v[2:3], v[2:3], v[126:127]
	v_pk_add_f32 v[0:1], v[0:1], v[124:125]
	s_cmp_lt_u32 s0, 9
	s_cbranch_scc1 .Lslab2_d
	v_pk_add_f32 v[4:5], v[4:5], v[130:131]
	v_pk_add_f32 v[8:9], v[8:9], v[128:129]
	v_pk_add_f32 v[2:3], v[2:3], v[134:135]
	v_pk_add_f32 v[0:1], v[0:1], v[132:133]
	s_cmp_lt_u32 s0, 10
	s_cbranch_scc1 .Lslab2_d
	v_pk_add_f32 v[4:5], v[4:5], v[138:139]
	v_pk_add_f32 v[8:9], v[8:9], v[136:137]
	v_pk_add_f32 v[2:3], v[2:3], v[142:143]
	v_pk_add_f32 v[0:1], v[0:1], v[140:141]
	s_cmp_lt_u32 s0, 11
	s_cbranch_scc1 .Lslab2_d
	v_pk_add_f32 v[4:5], v[4:5], v[146:147]
	v_pk_add_f32 v[8:9], v[8:9], v[144:145]
	v_pk_add_f32 v[2:3], v[2:3], v[150:151]
	v_pk_add_f32 v[0:1], v[0:1], v[148:149]
	s_cmp_lt_u32 s0, 12
	s_cbranch_scc1 .Lslab2_d
	v_pk_add_f32 v[4:5], v[4:5], v[154:155]
	v_pk_add_f32 v[8:9], v[8:9], v[152:153]
	v_pk_add_f32 v[2:3], v[2:3], v[158:159]
	v_pk_add_f32 v[0:1], v[0:1], v[156:157]
	s_cmp_lt_u32 s0, 13
	s_cbranch_scc1 .Lslab2_d
	v_pk_add_f32 v[4:5], v[4:5], v[162:163]
	v_pk_add_f32 v[8:9], v[8:9], v[160:161]
	v_pk_add_f32 v[2:3], v[2:3], v[166:167]
	v_pk_add_f32 v[0:1], v[0:1], v[164:165]
	s_cmp_lt_u32 s0, 14
	s_cbranch_scc1 .Lslab2_d
	v_pk_add_f32 v[4:5], v[4:5], v[170:171]
	v_pk_add_f32 v[8:9], v[8:9], v[168:169]
	v_pk_add_f32 v[2:3], v[2:3], v[174:175]
	v_pk_add_f32 v[0:1], v[0:1], v[172:173]
.Lslab2_d:
	s_mov_b32 s0, 0
	s_cmp_lg_u32 s0, 0
	v_pk_mul_f32 v[6:7], v[2:3], s[12:13] op_sel_hi:[1,0]
	v_pk_mul_f32 v[2:3], v[4:5], s[12:13] op_sel_hi:[1,0]
	v_pk_mul_f32 v[4:5], v[0:1], s[12:13] op_sel_hi:[1,0]
	v_pk_mul_f32 v[0:1], v[8:9], s[12:13] op_sel_hi:[1,0]
	s_mov_b64 s[0:1], 0

.LBB0_4043:
	global_load_dwordx4 v[64:67], v[14:15], off
	global_load_dwordx4 v[68:71], v[14:15], off offset:16
	s_cmp_lt_u32 s21, 2
	s_cbranch_scc1 .Lslab3_w
	v_lshl_add_u64 v[14:15], v[14:15], 0, s[10:11]
	global_load_dwordx4 v[72:75], v[14:15], off
	global_load_dwordx4 v[76:79], v[14:15], off offset:16
	s_cmp_lt_u32 s21, 3
	s_cbranch_scc1 .Lslab3_w
	v_lshl_add_u64 v[14:15], v[14:15], 0, s[10:11]
	global_load_dwordx4 v[80:83], v[14:15], off
	global_load_dwordx4 v[84:87], v[14:15], off offset:16
	s_cmp_lt_u32 s21, 4
	s_cbranch_scc1 .Lslab3_w
	v_lshl_add_u64 v[14:15], v[14:15], 0, s[10:11]
	global_load_dwordx4 v[88:91], v[14:15], off
	global_load_dwordx4 v[92:95], v[14:15], off offset:16
	s_cmp_lt_u32 s21, 5
	s_cbranch_scc1 .Lslab3_w
	v_lshl_add_u64 v[14:15], v[14:15], 0, s[10:11]
	global_load_dwordx4 v[96:99], v[14:15], off
	global_load_dwordx4 v[100:103], v[14:15], off offset:16
	s_cmp_lt_u32 s21, 6
	s_cbranch_scc1 .Lslab3_w
	v_lshl_add_u64 v[14:15], v[14:15], 0, s[10:11]
	global_load_dwordx4 v[104:107], v[14:15], off
	global_load_dwordx4 v[108:111], v[14:15], off offset:16
	s_cmp_lt_u32 s21, 7
	s_cbranch_scc1 .Lslab3_w
	v_lshl_add_u64 v[14:15], v[14:15], 0, s[10:11]
	global_load_dwordx4 v[112:115], v[14:15], off
	global_load_dwordx4 v[116:119], v[14:15], off offset:16
	s_cmp_lt_u32 s21, 8
	s_cbranch_scc1 .Lslab3_w
	v_lshl_add_u64 v[14:15], v[14:15], 0, s[10:11]
	global_load_dwordx4 v[120:123], v[14:15], off
	global_load_dwordx4 v[124:127], v[14:15], off offset:16
	s_cmp_lt_u32 s21, 9
	s_cbranch_scc1 .Lslab3_w
	v_lshl_add_u64 v[14:15], v[14:15], 0, s[10:11]
	global_load_dwordx4 v[128:131], v[14:15], off
	global_load_dwordx4 v[132:135], v[14:15], off offset:16
	s_cmp_lt_u32 s21, 10
	s_cbranch_scc1 .Lslab3_w
	v_lshl_add_u64 v[14:15], v[14:15], 0, s[10:11]
	global_load_dwordx4 v[136:139], v[14:15], off
	global_load_dwordx4 v[140:143], v[14:15], off offset:16
	s_cmp_lt_u32 s21, 11
	s_cbranch_scc1 .Lslab3_w
	v_lshl_add_u64 v[14:15], v[14:15], 0, s[10:11]
	global_load_dwordx4 v[144:147], v[14:15], off
	global_load_dwordx4 v[148:151], v[14:15], off offset:16
	s_cmp_lt_u32 s21, 12
	s_cbranch_scc1 .Lslab3_w
	v_lshl_add_u64 v[14:15], v[14:15], 0, s[10:11]
	global_load_dwordx4 v[152:155], v[14:15], off
	global_load_dwordx4 v[156:159], v[14:15], off offset:16
	s_cmp_lt_u32 s21, 13
	s_cbranch_scc1 .Lslab3_w
	v_lshl_add_u64 v[14:15], v[14:15], 0, s[10:11]
	global_load_dwordx4 v[160:163], v[14:15], off
	global_load_dwordx4 v[164:167], v[14:15], off offset:16
	s_cmp_lt_u32 s21, 14
	s_cbranch_scc1 .Lslab3_w
	v_lshl_add_u64 v[14:15], v[14:15], 0, s[10:11]
	global_load_dwordx4 v[168:171], v[14:15], off
	global_load_dwordx4 v[172:175], v[14:15], off offset:16
.Lslab3_w:
	s_waitcnt vmcnt(0)
	v_pk_add_f32 v[12:13], v[12:13], v[66:67]
	v_pk_add_f32 v[18:19], v[18:19], v[64:65]
	v_pk_add_f32 v[10:11], v[10:11], v[70:71]
	v_pk_add_f32 v[8:9], v[8:9], v[68:69]
	s_cmp_lt_u32 s21, 2
	s_cbranch_scc1 .Lslab3_d
	v_pk_add_f32 v[12:13], v[12:13], v[74:75]
	v_pk_add_f32 v[18:19], v[18:19], v[72:73]
	v_pk_add_f32 v[10:11], v[10:11], v[78:79]
	v_pk_add_f32 v[8:9], v[8:9], v[76:77]
	s_cmp_lt_u32 s21, 3
	s_cbranch_scc1 .Lslab3_d
	v_pk_add_f32 v[12:13], v[12:13], v[82:83]
	v_pk_add_f32 v[18:19], v[18:19], v[80:81]
	v_pk_add_f32 v[10:11], v[10:11], v[86:87]
	v_pk_add_f32 v[8:9], v[8:9], v[84:85]
	s_cmp_lt_u32 s21, 4
	s_cbranch_scc1 .Lslab3_d
	v_pk_add_f32 v[12:13], v[12:13], v[90:91]
	v_pk_add_f32 v[18:19], v[18:19], v[88:89]
	v_pk_add_f32 v[10:11], v[10:11], v[94:95]
	v_pk_add_f32 v[8:9], v[8:9], v[92:93]
	s_cmp_lt_u32 s21, 5
	s_cbranch_scc1 .Lslab3_d
	v_pk_add_f32 v[12:13], v[12:13], v[98:99]
	v_pk_add_f32 v[18:19], v[18:19], v[96:97]
	v_pk_add_f32 v[10:11], v[10:11], v[102:103]
	v_pk_add_f32 v[8:9], v[8:9], v[100:101]
	s_cmp_lt_u32 s21, 6
	s_cbranch_scc1 .Lslab3_d
	v_pk_add_f32 v[12:13], v[12:13], v[106:107]
	v_pk_add_f32 v[18:19], v[18:19], v[104:105]
	v_pk_add_f32 v[10:11], v[10:11], v[110:111]
	v_pk_add_f32 v[8:9], v[8:9], v[108:109]
	s_cmp_lt_u32 s21, 7
	s_cbranch_scc1 .Lslab3_d
	v_pk_add_f32 v[12:13], v[12:13], v[114:115]
	v_pk_add_f32 v[18:19], v[18:19], v[112:113]
	v_pk_add_f32 v[10:11], v[10:11], v[118:119]
	v_pk_add_f32 v[8:9], v[8:9], v[116:117]
	s_cmp_lt_u32 s21, 8
	s_cbranch_scc1 .Lslab3_d
	v_pk_add_f32 v[12:13], v[12:13], v[122:123]
	v_pk_add_f32 v[18:19], v[18:19], v[120:121]
	v_pk_add_f32 v[10:11], v[10:11], v[126:127]
	v_pk_add_f32 v[8:9], v[8:9], v[124:125]
	s_cmp_lt_u32 s21, 9
	s_cbranch_scc1 .Lslab3_d
	v_pk_add_f32 v[12:13], v[12:13], v[130:131]
	v_pk_add_f32 v[18:19], v[18:19], v[128:129]
	v_pk_add_f32 v[10:11], v[10:11], v[134:135]
	v_pk_add_f32 v[8:9], v[8:9], v[132:133]
	s_cmp_lt_u32 s21, 10
	s_cbranch_scc1 .Lslab3_d
	v_pk_add_f32 v[12:13], v[12:13], v[138:139]
	v_pk_add_f32 v[18:19], v[18:19], v[136:137]
	v_pk_add_f32 v[10:11], v[10:11], v[142:143]
	v_pk_add_f32 v[8:9], v[8:9], v[140:141]
	s_cmp_lt_u32 s21, 11
	s_cbranch_scc1 .Lslab3_d
	v_pk_add_f32 v[12:13], v[12:13], v[146:147]
	v_pk_add_f32 v[18:19], v[18:19], v[144:145]
	v_pk_add_f32 v[10:11], v[10:11], v[150:151]
	v_pk_add_f32 v[8:9], v[8:9], v[148:149]
	s_cmp_lt_u32 s21, 12
	s_cbranch_scc1 .Lslab3_d
	v_pk_add_f32 v[12:13], v[12:13], v[154:155]
	v_pk_add_f32 v[18:19], v[18:19], v[152:153]
	v_pk_add_f32 v[10:11], v[10:11], v[158:159]
	v_pk_add_f32 v[8:9], v[8:9], v[156:157]
	s_cmp_lt_u32 s21, 13
	s_cbranch_scc1 .Lslab3_d
	v_pk_add_f32 v[12:13], v[12:13], v[162:163]
	v_pk_add_f32 v[18:19], v[18:19], v[160:161]
	v_pk_add_f32 v[10:11], v[10:11], v[166:167]
	v_pk_add_f32 v[8:9], v[8:9], v[164:165]
	s_cmp_lt_u32 s21, 14
	s_cbranch_scc1 .Lslab3_d
	v_pk_add_f32 v[12:13], v[12:13], v[170:171]
	v_pk_add_f32 v[18:19], v[18:19], v[168:169]
	v_pk_add_f32 v[10:11], v[10:11], v[174:175]
	v_pk_add_f32 v[8:9], v[8:9], v[172:173]
.Lslab3_d:
	s_mov_b32 s21, 0
	s_cmp_lg_u32 s21, 0
	v_pk_mul_f32 v[14:15], v[10:11], s[12:13] op_sel_hi:[1,0]
	v_pk_mul_f32 v[10:11], v[12:13], s[12:13] op_sel_hi:[1,0]
	v_pk_mul_f32 v[12:13], v[8:9], s[12:13] op_sel_hi:[1,0]
	v_pk_mul_f32 v[8:9], v[18:19], s[12:13] op_sel_hi:[1,0]
	s_mov_b64 s[36:37], 0

.LBB0_4049:
	global_load_dwordx4 v[64:67], v[6:7], off
	global_load_dwordx4 v[68:71], v[6:7], off offset:16
	s_cmp_lt_u32 s21, 2
	s_cbranch_scc1 .Lslab4_w
	v_lshl_add_u64 v[6:7], v[6:7], 0, s[10:11]
	global_load_dwordx4 v[72:75], v[6:7], off
	global_load_dwordx4 v[76:79], v[6:7], off offset:16
	s_cmp_lt_u32 s21, 3
	s_cbranch_scc1 .Lslab4_w
	v_lshl_add_u64 v[6:7], v[6:7], 0, s[10:11]
	global_load_dwordx4 v[80:83], v[6:7], off
	global_load_dwordx4 v[84:87], v[6:7], off offset:16
	s_cmp_lt_u32 s21, 4
	s_cbranch_scc1 .Lslab4_w
	v_lshl_add_u64 v[6:7], v[6:7], 0, s[10:11]
	global_load_dwordx4 v[88:91], v[6:7], off
	global_load_dwordx4 v[92:95], v[6:7], off offset:16
	s_cmp_lt_u32 s21, 5
	s_cbranch_scc1 .Lslab4_w
	v_lshl_add_u64 v[6:7], v[6:7], 0, s[10:11]
	global_load_dwordx4 v[96:99], v[6:7], off
	global_load_dwordx4 v[100:103], v[6:7], off offset:16
	s_cmp_lt_u32 s21, 6
	s_cbranch_scc1 .Lslab4_w
	v_lshl_add_u64 v[6:7], v[6:7], 0, s[10:11]
	global_load_dwordx4 v[104:107], v[6:7], off
	global_load_dwordx4 v[108:111], v[6:7], off offset:16
	s_cmp_lt_u32 s21, 7
	s_cbranch_scc1 .Lslab4_w
	v_lshl_add_u64 v[6:7], v[6:7], 0, s[10:11]
	global_load_dwordx4 v[112:115], v[6:7], off
	global_load_dwordx4 v[116:119], v[6:7], off offset:16
	s_cmp_lt_u32 s21, 8
	s_cbranch_scc1 .Lslab4_w
	v_lshl_add_u64 v[6:7], v[6:7], 0, s[10:11]
	global_load_dwordx4 v[120:123], v[6:7], off
	global_load_dwordx4 v[124:127], v[6:7], off offset:16
	s_cmp_lt_u32 s21, 9
	s_cbranch_scc1 .Lslab4_w
	v_lshl_add_u64 v[6:7], v[6:7], 0, s[10:11]
	global_load_dwordx4 v[128:131], v[6:7], off
	global_load_dwordx4 v[132:135], v[6:7], off offset:16
	s_cmp_lt_u32 s21, 10
	s_cbranch_scc1 .Lslab4_w
	v_lshl_add_u64 v[6:7], v[6:7], 0, s[10:11]
	global_load_dwordx4 v[136:139], v[6:7], off
	global_load_dwordx4 v[140:143], v[6:7], off offset:16
	s_cmp_lt_u32 s21, 11
	s_cbranch_scc1 .Lslab4_w
	v_lshl_add_u64 v[6:7], v[6:7], 0, s[10:11]
	global_load_dwordx4 v[144:147], v[6:7], off
	global_load_dwordx4 v[148:151], v[6:7], off offset:16
	s_cmp_lt_u32 s21, 12
	s_cbranch_scc1 .Lslab4_w
	v_lshl_add_u64 v[6:7], v[6:7], 0, s[10:11]
	global_load_dwordx4 v[152:155], v[6:7], off
	global_load_dwordx4 v[156:159], v[6:7], off offset:16
	s_cmp_lt_u32 s21, 13
	s_cbranch_scc1 .Lslab4_w
	v_lshl_add_u64 v[6:7], v[6:7], 0, s[10:11]
	global_load_dwordx4 v[160:163], v[6:7], off
	global_load_dwordx4 v[164:167], v[6:7], off offset:16
	s_cmp_lt_u32 s21, 14
	s_cbranch_scc1 .Lslab4_w
	v_lshl_add_u64 v[6:7], v[6:7], 0, s[10:11]
	global_load_dwordx4 v[168:171], v[6:7], off
	global_load_dwordx4 v[172:175], v[6:7], off offset:16
.Lslab4_w:
	s_waitcnt vmcnt(0)
	v_pk_add_f32 v[4:5], v[4:5], v[66:67]
	v_pk_add_f32 v[8:9], v[8:9], v[64:65]
	v_pk_add_f32 v[2:3], v[2:3], v[70:71]
	v_pk_add_f32 v[0:1], v[0:1], v[68:69]
	s_cmp_lt_u32 s21, 2
	s_cbranch_scc1 .Lslab4_d
	v_pk_add_f32 v[4:5], v[4:5], v[74:75]
	v_pk_add_f32 v[8:9], v[8:9], v[72:73]
	v_pk_add_f32 v[2:3], v[2:3], v[78:79]
	v_pk_add_f32 v[0:1], v[0:1], v[76:77]
	s_cmp_lt_u32 s21, 3
	s_cbranch_scc1 .Lslab4_d
	v_pk_add_f32 v[4:5], v[4:5], v[82:83]
	v_pk_add_f32 v[8:9], v[8:9], v[80:81]
	v_pk_add_f32 v[2:3], v[2:3], v[86:87]
	v_pk_add_f32 v[0:1], v[0:1], v[84:85]
	s_cmp_lt_u32 s21, 4
	s_cbranch_scc1 .Lslab4_d
	v_pk_add_f32 v[4:5], v[4:5], v[90:91]
	v_pk_add_f32 v[8:9], v[8:9], v[88:89]
	v_pk_add_f32 v[2:3], v[2:3], v[94:95]
	v_pk_add_f32 v[0:1], v[0:1], v[92:93]
	s_cmp_lt_u32 s21, 5
	s_cbranch_scc1 .Lslab4_d
	v_pk_add_f32 v[4:5], v[4:5], v[98:99]
	v_pk_add_f32 v[8:9], v[8:9], v[96:97]
	v_pk_add_f32 v[2:3], v[2:3], v[102:103]
	v_pk_add_f32 v[0:1], v[0:1], v[100:101]
	s_cmp_lt_u32 s21, 6
	s_cbranch_scc1 .Lslab4_d
	v_pk_add_f32 v[4:5], v[4:5], v[106:107]
	v_pk_add_f32 v[8:9], v[8:9], v[104:105]
	v_pk_add_f32 v[2:3], v[2:3], v[110:111]
	v_pk_add_f32 v[0:1], v[0:1], v[108:109]
	s_cmp_lt_u32 s21, 7
	s_cbranch_scc1 .Lslab4_d
	v_pk_add_f32 v[4:5], v[4:5], v[114:115]
	v_pk_add_f32 v[8:9], v[8:9], v[112:113]
	v_pk_add_f32 v[2:3], v[2:3], v[118:119]
	v_pk_add_f32 v[0:1], v[0:1], v[116:117]
	s_cmp_lt_u32 s21, 8
	s_cbranch_scc1 .Lslab4_d
	v_pk_add_f32 v[4:5], v[4:5], v[122:123]
	v_pk_add_f32 v[8:9], v[8:9], v[120:121]
	v_pk_add_f32 v[2:3], v[2:3], v[126:127]
	v_pk_add_f32 v[0:1], v[0:1], v[124:125]
	s_cmp_lt_u32 s21, 9
	s_cbranch_scc1 .Lslab4_d
	v_pk_add_f32 v[4:5], v[4:5], v[130:131]
	v_pk_add_f32 v[8:9], v[8:9], v[128:129]
	v_pk_add_f32 v[2:3], v[2:3], v[134:135]
	v_pk_add_f32 v[0:1], v[0:1], v[132:133]
	s_cmp_lt_u32 s21, 10
	s_cbranch_scc1 .Lslab4_d
	v_pk_add_f32 v[4:5], v[4:5], v[138:139]
	v_pk_add_f32 v[8:9], v[8:9], v[136:137]
	v_pk_add_f32 v[2:3], v[2:3], v[142:143]
	v_pk_add_f32 v[0:1], v[0:1], v[140:141]
	s_cmp_lt_u32 s21, 11
	s_cbranch_scc1 .Lslab4_d
	v_pk_add_f32 v[4:5], v[4:5], v[146:147]
	v_pk_add_f32 v[8:9], v[8:9], v[144:145]
	v_pk_add_f32 v[2:3], v[2:3], v[150:151]
	v_pk_add_f32 v[0:1], v[0:1], v[148:149]
	s_cmp_lt_u32 s21, 12
	s_cbranch_scc1 .Lslab4_d
	v_pk_add_f32 v[4:5], v[4:5], v[154:155]
	v_pk_add_f32 v[8:9], v[8:9], v[152:153]
	v_pk_add_f32 v[2:3], v[2:3], v[158:159]
	v_pk_add_f32 v[0:1], v[0:1], v[156:157]
	s_cmp_lt_u32 s21, 13
	s_cbranch_scc1 .Lslab4_d
	v_pk_add_f32 v[4:5], v[4:5], v[162:163]
	v_pk_add_f32 v[8:9], v[8:9], v[160:161]
	v_pk_add_f32 v[2:3], v[2:3], v[166:167]
	v_pk_add_f32 v[0:1], v[0:1], v[164:165]
	s_cmp_lt_u32 s21, 14
	s_cbranch_scc1 .Lslab4_d
	v_pk_add_f32 v[4:5], v[4:5], v[170:171]
	v_pk_add_f32 v[8:9], v[8:9], v[168:169]
	v_pk_add_f32 v[2:3], v[2:3], v[174:175]
	v_pk_add_f32 v[0:1], v[0:1], v[172:173]
.Lslab4_d:
	s_mov_b32 s21, 0
	s_cmp_lg_u32 s21, 0
	v_pk_mul_f32 v[6:7], v[2:3], s[12:13] op_sel_hi:[1,0]
	v_pk_mul_f32 v[2:3], v[4:5], s[12:13] op_sel_hi:[1,0]
	v_pk_mul_f32 v[4:5], v[0:1], s[12:13] op_sel_hi:[1,0]
	v_pk_mul_f32 v[0:1], v[8:9], s[12:13] op_sel_hi:[1,0]

.Lslab5_w:
	s_waitcnt vmcnt(0)
	v_pk_add_f32 v[12:13], v[12:13], v[66:67]
	v_pk_add_f32 v[22:23], v[22:23], v[64:65]
	v_pk_add_f32 v[10:11], v[10:11], v[70:71]
	v_pk_add_f32 v[8:9], v[8:9], v[68:69]
	s_cmp_lt_u32 s21, 2
	s_cbranch_scc1 .Lslab5_d
	v_pk_add_f32 v[12:13], v[12:13], v[74:75]
	v_pk_add_f32 v[22:23], v[22:23], v[72:73]
	v_pk_add_f32 v[10:11], v[10:11], v[78:79]
	v_pk_add_f32 v[8:9], v[8:9], v[76:77]
	s_cmp_lt_u32 s21, 3
	s_cbranch_scc1 .Lslab5_d
	v_pk_add_f32 v[12:13], v[12:13], v[82:83]
	v_pk_add_f32 v[22:23], v[22:23], v[80:81]
	v_pk_add_f32 v[10:11], v[10:11], v[86:87]
	v_pk_add_f32 v[8:9], v[8:9], v[84:85]
	s_cmp_lt_u32 s21, 4
	s_cbranch_scc1 .Lslab5_d
	v_pk_add_f32 v[12:13], v[12:13], v[90:91]
	v_pk_add_f32 v[22:23], v[22:23], v[88:89]
	v_pk_add_f32 v[10:11], v[10:11], v[94:95]
	v_pk_add_f32 v[8:9], v[8:9], v[92:93]
	s_cmp_lt_u32 s21, 5
	s_cbranch_scc1 .Lslab5_d
	v_pk_add_f32 v[12:13], v[12:13], v[98:99]
	v_pk_add_f32 v[22:23], v[22:23], v[96:97]
	v_pk_add_f32 v[10:11], v[10:11], v[102:103]
	v_pk_add_f32 v[8:9], v[8:9], v[100:101]
	s_cmp_lt_u32 s21, 6
	s_cbranch_scc1 .Lslab5_d
	v_pk_add_f32 v[12:13], v[12:13], v[106:107]
	v_pk_add_f32 v[22:23], v[22:23], v[104:105]
	v_pk_add_f32 v[10:11], v[10:11], v[110:111]
	v_pk_add_f32 v[8:9], v[8:9], v[108:109]
	s_cmp_lt_u32 s21, 7
	s_cbranch_scc1 .Lslab5_d
	v_pk_add_f32 v[12:13], v[12:13], v[114:115]
	v_pk_add_f32 v[22:23], v[22:23], v[112:113]
	v_pk_add_f32 v[10:11], v[10:11], v[118:119]
	v_pk_add_f32 v[8:9], v[8:9], v[116:117]
	s_cmp_lt_u32 s21, 8
	s_cbranch_scc1 .Lslab5_d
	v_pk_add_f32 v[12:13], v[12:13], v[122:123]
	v_pk_add_f32 v[22:23], v[22:23], v[120:121]
	v_pk_add_f32 v[10:11], v[10:11], v[126:127]
	v_pk_add_f32 v[8:9], v[8:9], v[124:125]
	s_cmp_lt_u32 s21, 9
	s_cbranch_scc1 .Lslab5_d
	v_pk_add_f32 v[12:13], v[12:13], v[130:131]
	v_pk_add_f32 v[22:23], v[22:23], v[128:129]
	v_pk_add_f32 v[10:11], v[10:11], v[134:135]
	v_pk_add_f32 v[8:9], v[8:9], v[132:133]
	s_cmp_lt_u32 s21, 10
	s_cbranch_scc1 .Lslab5_d
	v_pk_add_f32 v[12:13], v[12:13], v[138:139]
	v_pk_add_f32 v[22:23], v[22:23], v[136:137]
	v_pk_add_f32 v[10:11], v[10:11], v[142:143]
	v_pk_add_f32 v[8:9], v[8:9], v[140:141]
	s_cmp_lt_u32 s21, 11
	s_cbranch_scc1 .Lslab5_d
	v_pk_add_f32 v[12:13], v[12:13], v[146:147]
	v_pk_add_f32 v[22:23], v[22:23], v[144:145]
	v_pk_add_f32 v[10:11], v[10:11], v[150:151]
	v_pk_add_f32 v[8:9], v[8:9], v[148:149]
	s_cmp_lt_u32 s21, 12
	s_cbranch_scc1 .Lslab5_d
	v_pk_add_f32 v[12:13], v[12:13], v[154:155]
	v_pk_add_f32 v[22:23], v[22:23], v[152:153]
	v_pk_add_f32 v[10:11], v[10:11], v[158:159]
	v_pk_add_f32 v[8:9], v[8:9], v[156:157]
	s_cmp_lt_u32 s21, 13
	s_cbranch_scc1 .Lslab5_d
	v_pk_add_f32 v[12:13], v[12:13], v[162:163]
	v_pk_add_f32 v[22:23], v[22:23], v[160:161]
	v_pk_add_f32 v[10:11], v[10:11], v[166:167]
	v_pk_add_f32 v[8:9], v[8:9], v[164:165]
	s_cmp_lt_u32 s21, 14
	s_cbranch_scc1 .Lslab5_d
	v_pk_add_f32 v[12:13], v[12:13], v[170:171]
	v_pk_add_f32 v[22:23], v[22:23], v[168:169]
	v_pk_add_f32 v[10:11], v[10:11], v[174:175]
	v_pk_add_f32 v[8:9], v[8:9], v[172:173]
.Lslab5_d:
	s_mov_b32 s21, 0
	s_cmp_lg_u32 s21, 0
	v_pk_mul_f32 v[14:15], v[10:11], s[12:13] op_sel_hi:[1,0]
	v_pk_mul_f32 v[10:11], v[12:13], s[12:13] op_sel_hi:[1,0]
	v_pk_mul_f32 v[12:13], v[8:9], s[12:13] op_sel_hi:[1,0]
	v_pk_mul_f32 v[8:9], v[22:23], s[12:13] op_sel_hi:[1,0]
	s_branch .LBB0_4059

.Lslab6_d:
	s_mov_b32 s2, 0
	s_cmp_lg_u32 s2, 0
	v_pk_mul_f32 v[6:7], v[2:3], s[12:13] op_sel_hi:[1,0]
	v_pk_mul_f32 v[2:3], v[4:5], s[12:13] op_sel_hi:[1,0]
	v_pk_mul_f32 v[4:5], v[0:1], s[12:13] op_sel_hi:[1,0]
	v_pk_mul_f32 v[0:1], v[8:9], s[12:13] op_sel_hi:[1,0]

.LBB0_4065:
	global_load_dwordx4 v[64:67], v[14:15], off
	global_load_dwordx4 v[68:71], v[14:15], off offset:16
	s_cmp_lt_u32 s0, 2
	s_cbranch_scc1 .Lslab7_w
	v_lshl_add_u64 v[14:15], v[14:15], 0, s[10:11]
	global_load_dwordx4 v[72:75], v[14:15], off
	global_load_dwordx4 v[76:79], v[14:15], off offset:16
	s_cmp_lt_u32 s0, 3
	s_cbranch_scc1 .Lslab7_w
	v_lshl_add_u64 v[14:15], v[14:15], 0, s[10:11]
	global_load_dwordx4 v[80:83], v[14:15], off
	global_load_dwordx4 v[84:87], v[14:15], off offset:16
	s_cmp_lt_u32 s0, 4
	s_cbranch_scc1 .Lslab7_w
	v_lshl_add_u64 v[14:15], v[14:15], 0, s[10:11]
	global_load_dwordx4 v[88:91], v[14:15], off
	global_load_dwordx4 v[92:95], v[14:15], off offset:16
	s_cmp_lt_u32 s0, 5
	s_cbranch_scc1 .Lslab7_w
	v_lshl_add_u64 v[14:15], v[14:15], 0, s[10:11]
	global_load_dwordx4 v[96:99], v[14:15], off
	global_load_dwordx4 v[100:103], v[14:15], off offset:16
	s_cmp_lt_u32 s0, 6
	s_cbranch_scc1 .Lslab7_w
	v_lshl_add_u64 v[14:15], v[14:15], 0, s[10:11]
	global_load_dwordx4 v[104:107], v[14:15], off
	global_load_dwordx4 v[108:111], v[14:15], off offset:16
	s_cmp_lt_u32 s0, 7
	s_cbranch_scc1 .Lslab7_w
	v_lshl_add_u64 v[14:15], v[14:15], 0, s[10:11]
	global_load_dwordx4 v[112:115], v[14:15], off
	global_load_dwordx4 v[116:119], v[14:15], off offset:16
	s_cmp_lt_u32 s0, 8
	s_cbranch_scc1 .Lslab7_w
	v_lshl_add_u64 v[14:15], v[14:15], 0, s[10:11]
	global_load_dwordx4 v[120:123], v[14:15], off
	global_load_dwordx4 v[124:127], v[14:15], off offset:16
	s_cmp_lt_u32 s0, 9
	s_cbranch_scc1 .Lslab7_w
	v_lshl_add_u64 v[14:15], v[14:15], 0, s[10:11]
	global_load_dwordx4 v[128:131], v[14:15], off
	global_load_dwordx4 v[132:135], v[14:15], off offset:16
	s_cmp_lt_u32 s0, 10
	s_cbranch_scc1 .Lslab7_w
	v_lshl_add_u64 v[14:15], v[14:15], 0, s[10:11]
	global_load_dwordx4 v[136:139], v[14:15], off
	global_load_dwordx4 v[140:143], v[14:15], off offset:16
	s_cmp_lt_u32 s0, 11
	s_cbranch_scc1 .Lslab7_w
	v_lshl_add_u64 v[14:15], v[14:15], 0, s[10:11]
	global_load_dwordx4 v[144:147], v[14:15], off
	global_load_dwordx4 v[148:151], v[14:15], off offset:16
	s_cmp_lt_u32 s0, 12
	s_cbranch_scc1 .Lslab7_w
	v_lshl_add_u64 v[14:15], v[14:15], 0, s[10:11]
	global_load_dwordx4 v[152:155], v[14:15], off
	global_load_dwordx4 v[156:159], v[14:15], off offset:16
	s_cmp_lt_u32 s0, 13
	s_cbranch_scc1 .Lslab7_w
	v_lshl_add_u64 v[14:15], v[14:15], 0, s[10:11]
	global_load_dwordx4 v[160:163], v[14:15], off
	global_load_dwordx4 v[164:167], v[14:15], off offset:16
	s_cmp_lt_u32 s0, 14
	s_cbranch_scc1 .Lslab7_w
	v_lshl_add_u64 v[14:15], v[14:15], 0, s[10:11]
	global_load_dwordx4 v[168:171], v[14:15], off
	global_load_dwordx4 v[172:175], v[14:15], off offset:16
.Lslab7_w:
	s_waitcnt vmcnt(0)
	v_pk_add_f32 v[12:13], v[12:13], v[66:67]
	v_pk_add_f32 v[22:23], v[22:23], v[64:65]
	v_pk_add_f32 v[10:11], v[10:11], v[70:71]
	v_pk_add_f32 v[8:9], v[8:9], v[68:69]
	s_cmp_lt_u32 s0, 2
	s_cbranch_scc1 .Lslab7_d
	v_pk_add_f32 v[12:13], v[12:13], v[74:75]
	v_pk_add_f32 v[22:23], v[22:23], v[72:73]
	v_pk_add_f32 v[10:11], v[10:11], v[78:79]
	v_pk_add_f32 v[8:9], v[8:9], v[76:77]
	s_cmp_lt_u32 s0, 3
	s_cbranch_scc1 .Lslab7_d
	v_pk_add_f32 v[12:13], v[12:13], v[82:83]
	v_pk_add_f32 v[22:23], v[22:23], v[80:81]
	v_pk_add_f32 v[10:11], v[10:11], v[86:87]
	v_pk_add_f32 v[8:9], v[8:9], v[84:85]
	s_cmp_lt_u32 s0, 4
	s_cbranch_scc1 .Lslab7_d
	v_pk_add_f32 v[12:13], v[12:13], v[90:91]
	v_pk_add_f32 v[22:23], v[22:23], v[88:89]
	v_pk_add_f32 v[10:11], v[10:11], v[94:95]
	v_pk_add_f32 v[8:9], v[8:9], v[92:93]
	s_cmp_lt_u32 s0, 5
	s_cbranch_scc1 .Lslab7_d
	v_pk_add_f32 v[12:13], v[12:13], v[98:99]
	v_pk_add_f32 v[22:23], v[22:23], v[96:97]
	v_pk_add_f32 v[10:11], v[10:11], v[102:103]
	v_pk_add_f32 v[8:9], v[8:9], v[100:101]
	s_cmp_lt_u32 s0, 6
	s_cbranch_scc1 .Lslab7_d
	v_pk_add_f32 v[12:13], v[12:13], v[106:107]
	v_pk_add_f32 v[22:23], v[22:23], v[104:105]
	v_pk_add_f32 v[10:11], v[10:11], v[110:111]
	v_pk_add_f32 v[8:9], v[8:9], v[108:109]
	s_cmp_lt_u32 s0, 7
	s_cbranch_scc1 .Lslab7_d
	v_pk_add_f32 v[12:13], v[12:13], v[114:115]
	v_pk_add_f32 v[22:23], v[22:23], v[112:113]
	v_pk_add_f32 v[10:11], v[10:11], v[118:119]
	v_pk_add_f32 v[8:9], v[8:9], v[116:117]
	s_cmp_lt_u32 s0, 8
	s_cbranch_scc1 .Lslab7_d
	v_pk_add_f32 v[12:13], v[12:13], v[122:123]
	v_pk_add_f32 v[22:23], v[22:23], v[120:121]
	v_pk_add_f32 v[10:11], v[10:11], v[126:127]
	v_pk_add_f32 v[8:9], v[8:9], v[124:125]
	s_cmp_lt_u32 s0, 9
	s_cbranch_scc1 .Lslab7_d
	v_pk_add_f32 v[12:13], v[12:13], v[130:131]
	v_pk_add_f32 v[22:23], v[22:23], v[128:129]
	v_pk_add_f32 v[10:11], v[10:11], v[134:135]
	v_pk_add_f32 v[8:9], v[8:9], v[132:133]
	s_cmp_lt_u32 s0, 10
	s_cbranch_scc1 .Lslab7_d
	v_pk_add_f32 v[12:13], v[12:13], v[138:139]
	v_pk_add_f32 v[22:23], v[22:23], v[136:137]
	v_pk_add_f32 v[10:11], v[10:11], v[142:143]
	v_pk_add_f32 v[8:9], v[8:9], v[140:141]
	s_cmp_lt_u32 s0, 11
	s_cbranch_scc1 .Lslab7_d
	v_pk_add_f32 v[12:13], v[12:13], v[146:147]
	v_pk_add_f32 v[22:23], v[22:23], v[144:145]
	v_pk_add_f32 v[10:11], v[10:11], v[150:151]
	v_pk_add_f32 v[8:9], v[8:9], v[148:149]
	s_cmp_lt_u32 s0, 12
	s_cbranch_scc1 .Lslab7_d
	v_pk_add_f32 v[12:13], v[12:13], v[154:155]
	v_pk_add_f32 v[22:23], v[22:23], v[152:153]
	v_pk_add_f32 v[10:11], v[10:11], v[158:159]
	v_pk_add_f32 v[8:9], v[8:9], v[156:157]
	s_cmp_lt_u32 s0, 13
	s_cbranch_scc1 .Lslab7_d
	v_pk_add_f32 v[12:13], v[12:13], v[162:163]
	v_pk_add_f32 v[22:23], v[22:23], v[160:161]
	v_pk_add_f32 v[10:11], v[10:11], v[166:167]
	v_pk_add_f32 v[8:9], v[8:9], v[164:165]
	s_cmp_lt_u32 s0, 14
	s_cbranch_scc1 .Lslab7_d
	v_pk_add_f32 v[12:13], v[12:13], v[170:171]
	v_pk_add_f32 v[22:23], v[22:23], v[168:169]
	v_pk_add_f32 v[10:11], v[10:11], v[174:175]
	v_pk_add_f32 v[8:9], v[8:9], v[172:173]
.Lslab7_d:
	s_mov_b32 s0, 0
	s_cmp_lg_u32 s0, 0
	v_pk_mul_f32 v[14:15], v[10:11], s[12:13] op_sel_hi:[1,0]
	v_pk_mul_f32 v[10:11], v[12:13], s[12:13] op_sel_hi:[1,0]
	v_pk_mul_f32 v[12:13], v[8:9], s[12:13] op_sel_hi:[1,0]
	v_pk_mul_f32 v[8:9], v[22:23], s[12:13] op_sel_hi:[1,0]
	s_branch .LBB0_4071
